# MLA attention units assigned by XCD-contiguous workgroup id so the 16 workgroups of a (batch,head) share one L2; plus VALU trims (no permlane)
# speedup vs baseline: 1.0053x; 1.0002x over previous
.LBB0_453:
	v_readlane_b32 s2, v239, 7
	v_readlane_b32 s3, v239, 8
	s_cmp_le_i32 s2, s36
	s_cselect_b64 s[0:1], -1, 0
	s_cmp_lt_i32 s36, s3
	s_cselect_b64 s[2:3], -1, 0
	s_and_b64 s[0:1], s[0:1], s[2:3]
	s_andn2_b64 vcc, exec, s[0:1]
	s_cbranch_vccnz .LBB0_529
	v_readlane_b32 s0, v239, 19
	v_readlane_b32 s1, v239, 20
	s_andn2_b64 vcc, exec, s[0:1]
	s_cbranch_vccnz .LBB0_483
	s_add_u32 s0, s78, 0xb400000
	s_addc_u32 s1, s79, 0
	s_add_u32 s28, s78, 0xe400000
	s_addc_u32 s29, s79, 0
	s_add_u32 s30, s78, 0xae00000
	s_addc_u32 s31, s79, 0
	s_add_u32 s34, s78, 0x10400000
	s_addc_u32 s35, s79, 0
	s_add_u32 s2, s78, 0xb000000
	s_addc_u32 s3, s79, 0
	s_mov_b32 s36, s92
	s_branch .LBB0_457

.LBB0_457:
	s_lshl_b32 s5, s36, 8
	s_and_b32 s37, s5, 0xf00
	s_ashr_i32 s4, s36, 7
	s_xor_b32 s7, s37, 0x1f00
	v_readlane_b32 s5, v239, 14
	s_mov_b64 s[18:19], s[78:79]
	s_waitcnt vmcnt(0)
	v_mov_b32_e32 v66, v0
	s_add_i32 s41, s7, s5
	s_ashr_i32 s5, s4, 31
	s_lshl_b64 s[10:11], s[4:5], 13
	v_and_or_b32 v166, v66, 31, s41
	s_bfe_u32 s6, s36, 0x30004
	v_lshl_add_u64 v[174:175], s[10:11], 0, v[166:167]
	s_waitcnt vmcnt(0) lgkmcnt(0)
	v_mov_b64_e32 v[2:3], s[0:1]
	s_movk_i32 s12, 0xc00
	v_mad_u64_u32 v[2:3], s[8:9], v174, s12, v[2:3]
	s_mul_i32 s40, s6, 0xc0
	v_bfe_u32 v1, v66, 5, 1
	v_mad_i32_i24 v3, v175, s12, v3
	s_lshl_b32 s84, s40, 1
	v_lshl_add_u64 v[2:3], v[2:3], 0, s[84:85]
	v_lshlrev_b32_e32 v172, 4, v1
	v_mov_b32_e32 v173, v167
	v_lshl_add_u64 v[48:49], v[2:3], 0, v[172:173]
	v_lshlrev_b64 v[6:7], 8, v[174:175]
	global_load_dwordx4 v[16:19], v[48:49], off offset:256
	global_load_dwordx4 v[2:5], v[48:49], off offset:320
	v_lshl_add_u64 v[6:7], s[2:3], 0, v[6:7]
	v_lshlrev_b32_e32 v14, 5, v1
	v_mov_b32_e32 v15, v167
	v_lshl_add_u64 v[40:41], v[6:7], 0, v[14:15]
	global_load_dwordx4 v[20:23], v[40:41], off offset:128
	global_load_dwordx4 v[6:9], v[40:41], off offset:144
	global_load_dwordx4 v[24:27], v[40:41], off
	global_load_dwordx4 v[10:13], v[40:41], off offset:16
	v_lshlrev_b32_e32 v1, 2, v66
	v_lshrrev_b32_e32 v15, 1, v66
	v_and_b32_e32 v28, 3, v66
	v_and_b32_e32 v15, 12, v15
	v_and_b32_e32 v69, 16, v1
	v_or3_b32 v15, v15, v28, v69
	global_load_dwordx4 v[28:31], v[40:41], off offset:80
	global_load_dwordx4 v[32:35], v[40:41], off offset:64
	global_load_dwordx4 v[36:39], v[40:41], off offset:208
	s_nop 0
	global_load_dwordx4 v[40:43], v[40:41], off offset:192
	s_nop 0
	global_load_dwordx4 v[98:101], v[48:49], off
	global_load_dwordx4 v[102:105], v[48:49], off offset:32
	global_load_dwordx4 v[106:109], v[48:49], off offset:64
	global_load_dwordx4 v[110:113], v[48:49], off offset:96
	global_load_dwordx4 v[114:117], v[48:49], off offset:128
	global_load_dwordx4 v[118:121], v[48:49], off offset:160
	global_load_dwordx4 v[122:125], v[48:49], off offset:192
	global_load_dwordx4 v[126:129], v[48:49], off offset:224
	global_load_dwordx4 v[44:47], v[48:49], off offset:288
	s_nop 0
	global_load_dwordx4 v[48:51], v[48:49], off offset:352
	v_lshlrev_b32_e32 v67, 6, v66
	v_lshlrev_b32_e32 v68, 3, v66
	s_lshl_b32 s21, s6, 22
	s_lshl_b32 s20, s6, 8
	s_add_i32 s22, s7, 0x100
	v_and_b32_e32 v70, 0x78, v68
	s_mov_b32 s7, 0x7ffffc00
	s_lshl_b64 s[8:9], s[4:5], 24
	v_and_or_b32 v1, v67, s7, v70
	s_mov_b32 s23, 0x7fffc000
	v_lshlrev_b32_e32 v1, 1, v1
	s_barrier
	s_mov_b32 s47, 0
	v_mov_b32_e32 v207, 0xf149f2ca
	v_mov_b32_e32 v205, 0
	s_mov_b32 s45, 63
	s_waitcnt vmcnt(19)
	v_lshlrev_b32_e32 v52, 16, v16
	v_and_b32_e32 v53, 0xffff0000, v16
	s_waitcnt vmcnt(18)
	v_lshlrev_b32_e32 v54, 16, v2
	v_and_b32_e32 v55, 0xffff0000, v2
	v_lshlrev_b32_e32 v16, 16, v17
	v_and_b32_e32 v17, 0xffff0000, v17
	v_lshlrev_b32_e32 v2, 16, v3
	v_and_b32_e32 v3, 0xffff0000, v3
	v_lshlrev_b32_e32 v56, 16, v18
	v_and_b32_e32 v57, 0xffff0000, v18
	v_lshlrev_b32_e32 v58, 16, v4
	v_and_b32_e32 v59, 0xffff0000, v4
	s_waitcnt vmcnt(17)
	v_pk_mul_f32 v[62:63], v[22:23], v[2:3]
	v_pk_mul_f32 v[22:23], v[22:23], v[16:17]
	s_waitcnt vmcnt(16)
	v_pk_mul_f32 v[64:65], v[6:7], v[58:59]
	v_pk_mul_f32 v[6:7], v[6:7], v[56:57]
	s_waitcnt vmcnt(15)
	v_pk_fma_f32 v[2:3], v[26:27], v[2:3], v[22:23]
	s_waitcnt vmcnt(14)
	v_pk_fma_f32 v[22:23], v[10:11], v[56:57], v[64:65] neg_lo:[0,0,1] neg_hi:[0,0,1]
	v_pk_fma_f32 v[6:7], v[10:11], v[58:59], v[6:7]
	v_add_u32_e32 v10, 0x8000, v67
	v_and_or_b32 v10, v10, s7, v70
	s_add_u32 s7, s28, s8
	v_lshlrev_b32_e32 v173, 1, v10
	v_lshlrev_b32_e32 v10, 11, v66
	v_and_b32_e32 v11, 56, v68
	s_addc_u32 s13, s29, s9
	s_lshl_b32 s42, s6, 7
	v_cvt_pk_bf16_f32 v132, v22, v23
	v_and_or_b32 v22, v10, s23, v11
	s_add_u32 s12, s7, s20
	v_lshlrev_b32_e32 v178, 1, v22
	s_addc_u32 s13, s13, 0
	v_mov_b32_e32 v22, v1
	global_load_dwordx4 v[134:137], v22, s[12:13]
	v_pk_fma_f32 v[16:17], v[26:27], v[16:17], v[62:63] neg_lo:[0,0,1] neg_hi:[0,0,1]
	s_lshl_b64 s[6:7], s[4:5], 20
	v_cvt_pk_bf16_f32 v131, v16, v17
	v_lshlrev_b32_e32 v17, 4, v66
	s_add_u32 s14, s30, s6
	v_ashrrev_i32_e32 v16, 3, v66
	v_and_b32_e32 v176, 0x70, v17
	s_addc_u32 s15, s31, s7
	v_mov_b32_e32 v22, v173
	v_lshl_or_b32 v177, v16, 7, v176
	s_add_u32 s16, s34, s21
	global_load_dwordx4 v[138:141], v22, s[12:13]
	s_addc_u32 s17, s35, 0
	s_lshl_b64 s[4:5], s[4:5], 14
	v_mov_b32_e32 v22, v177
	s_add_u32 s16, s16, s4
	v_add_u32_e32 v10, 0x100000, v10
	global_load_dwordx4 v[142:145], v22, s[14:15]
	s_addc_u32 s17, s17, s5
	v_mov_b32_e32 v22, v178
	v_and_or_b32 v10, v10, s23, v11
	global_load_dwordx4 v[154:157], v22, s[16:17]
	v_lshlrev_b32_e32 v179, 1, v10
	v_mov_b32_e32 v10, v179
	global_load_dwordx4 v[158:161], v10, s[16:17]
	v_lshlrev_b32_e32 v18, 16, v19
	v_and_b32_e32 v19, 0xffff0000, v19
	v_lshlrev_b32_e32 v4, 16, v5
	v_and_b32_e32 v5, 0xffff0000, v5
	v_pk_mul_f32 v[10:11], v[8:9], v[4:5]
	v_pk_mul_f32 v[8:9], v[8:9], v[18:19]
	v_cvt_pk_bf16_f32 v147, v2, v3
	v_pk_fma_f32 v[4:5], v[12:13], v[4:5], v[8:9]
	v_cvt_pk_bf16_f32 v148, v6, v7
	v_cvt_pk_bf16_f32 v149, v4, v5
	s_waitcnt vmcnt(5)
	v_lshlrev_b32_e32 v4, 16, v48
	v_and_b32_e32 v5, 0xffff0000, v48
	v_lshlrev_b32_e32 v2, 16, v44
	v_and_b32_e32 v3, 0xffff0000, v44
	v_pk_mul_f32 v[6:7], v[40:41], v[4:5]
	s_movk_i32 s23, 0x1a0
	v_pk_fma_f32 v[6:7], v[32:33], v[2:3], v[6:7] neg_lo:[0,0,1] neg_hi:[0,0,1]
	v_pk_mul_f32 v[2:3], v[40:41], v[2:3]
	v_and_b32_e32 v180, 0xf0, v17
	v_pk_fma_f32 v[2:3], v[32:33], v[4:5], v[2:3]
	v_cvt_pk_bf16_f32 v150, v6, v7
	v_cvt_pk_bf16_f32 v162, v2, v3
	v_ashrrev_i32_e32 v2, 4, v66
	v_mul_lo_u32 v181, v2, s23
	v_add_u32_e32 v3, 0, v181
	v_and_b32_e32 v182, 16, v2
	v_lshlrev_b32_e32 v6, 16, v49
	v_and_b32_e32 v7, 0xffff0000, v49
	v_add3_u32 v2, v3, v182, v180
	v_lshlrev_b32_e32 v4, 16, v45
	v_and_b32_e32 v5, 0xffff0000, v45
	v_pk_mul_f32 v[8:9], v[42:43], v[6:7]
	v_and_b32_e32 v185, 16, v16
	v_pk_fma_f32 v[8:9], v[34:35], v[4:5], v[8:9] neg_lo:[0,0,1] neg_hi:[0,0,1]
	v_pk_mul_f32 v[4:5], v[42:43], v[4:5]
	s_lshr_b32 s43, s22, 6
	v_pk_fma_f32 v[4:5], v[34:35], v[6:7], v[4:5]
	s_or_b32 s44, s41, 31
	v_cvt_pk_bf16_f32 v163, v4, v5
	v_pk_fma_f32 v[10:11], v[12:13], v[18:19], v[10:11] neg_lo:[0,0,1] neg_hi:[0,0,1]
	v_cvt_pk_bf16_f32 v151, v8, v9
	v_lshlrev_b32_e32 v8, 16, v50
	v_and_b32_e32 v9, 0xffff0000, v50
	s_add_u32 s4, s21, s4
	v_cvt_pk_bf16_f32 v133, v10, v11
	v_lshlrev_b32_e32 v6, 16, v46
	v_and_b32_e32 v7, 0xffff0000, v46
	v_pk_mul_f32 v[10:11], v[36:37], v[8:9]
	s_addc_u32 s5, 0, s5
	v_pk_fma_f32 v[10:11], v[28:29], v[6:7], v[10:11] neg_lo:[0,0,1] neg_hi:[0,0,1]
	s_waitcnt vmcnt(4)
	ds_write_b128 v2, v[134:137]
	v_add_u32_e32 v2, 0x200, v66
	v_ashrrev_i32_e32 v3, 4, v2
	v_mul_lo_u32 v183, v3, s23
	v_add_u32_e32 v4, 0, v183
	v_and_b32_e32 v184, 16, v3
	v_add3_u32 v3, v4, v184, v180
	v_lshlrev_b32_e32 v4, 8, v16
	v_ashrrev_i32_e32 v2, 3, v2
	v_and_b32_e32 v202, 16, v2
	s_add_u32 s4, s4, 0x10400080
	v_cvt_pk_bf16_f32 v152, v10, v11
	v_pk_mul_f32 v[6:7], v[36:37], v[6:7]
	s_waitcnt vmcnt(3)
	ds_write_b128 v3, v[138:141]
	v_mul_lo_u32 v3, v16, s23
	v_add3_u32 v3, 0, v3, v185
	v_add_u32_e32 v199, v3, v176
	s_movk_i32 s23, 0xa0
	v_sub_u32_e32 v3, v3, v4
	v_add_u32_e32 v3, v3, v176
	v_mul_lo_u32 v201, v2, s23
	s_waitcnt vmcnt(2)
	ds_write_b128 v199, v[142:145] offset:256
	v_lshlrev_b32_e32 v10, 16, v51
	v_and_b32_e32 v11, 0xffff0000, v51
	s_addc_u32 s5, s5, 0
	s_waitcnt vmcnt(1)
	ds_write_b128 v3, v[154:157] offset:53248
	v_add_u32_e32 v3, 0, v201
	v_add3_u32 v2, v3, v202, v176
	v_pk_fma_f32 v[6:7], v[28:29], v[8:9], v[6:7]
	v_lshlrev_b32_e32 v8, 16, v47
	v_and_b32_e32 v9, 0xffff0000, v47
	v_pk_mul_f32 v[12:13], v[38:39], v[10:11]
	s_waitcnt vmcnt(0)
	ds_write_b128 v2, v[158:161] offset:53248
	v_mul_u32_u24_e32 v2, 0x1a0, v15
	s_add_u32 s6, s6, 0xae02000
	v_pk_mul_f32 v[60:61], v[20:21], v[54:55]
	v_pk_mul_f32 v[20:21], v[20:21], v[52:53]
	v_pk_fma_f32 v[12:13], v[30:31], v[8:9], v[12:13] neg_lo:[0,0,1] neg_hi:[0,0,1]
	v_pk_mul_f32 v[8:9], v[38:39], v[8:9]
	v_add3_u32 v2, 0, v2, v69
	v_lshlrev_b32_e32 v3, 8, v15
	s_addc_u32 s7, s7, 0
	s_or_b32 s8, s8, s20
	v_pk_fma_f32 v[52:53], v[24:25], v[52:53], v[60:61] neg_lo:[0,0,1] neg_hi:[0,0,1]
	v_pk_fma_f32 v[20:21], v[24:25], v[54:55], v[20:21]
	v_pk_fma_f32 v[8:9], v[30:31], v[10:11], v[8:9]
	v_add_u32_e32 v203, v2, v172
	v_sub_u32_e32 v2, v2, v3
	s_add_u32 s8, s8, 0xe420000
	v_mov_b32_e32 v18, v167
	v_mov_b32_e32 v19, v167
	v_mov_b32_e32 v32, v167
	v_mov_b32_e32 v33, v167
	v_cvt_pk_bf16_f32 v130, v52, v53
	v_cvt_pk_bf16_f32 v146, v20, v21
	v_cvt_pk_bf16_f32 v153, v12, v13
	v_cvt_pk_bf16_f32 v164, v6, v7
	v_cvt_pk_bf16_f32 v165, v8, v9
	v_mul_lo_u32 v200, v16, s23
	v_add_u32_e32 v204, v2, v14
	s_addc_u32 s9, s9, 0
	v_mov_b32_e32 v20, v167
	v_mov_b32_e32 v21, v167
	v_mov_b32_e32 v22, v167
	v_mov_b32_e32 v23, v167
	v_mov_b32_e32 v24, v167
	v_mov_b32_e32 v25, v167
	v_mov_b32_e32 v26, v167
	v_mov_b32_e32 v27, v167
	v_mov_b32_e32 v28, v167
	v_mov_b32_e32 v29, v167
	v_mov_b32_e32 v30, v167
	v_mov_b32_e32 v31, v167
	v_mov_b64_e32 v[48:49], v[32:33]
	v_mov_b64_e32 v[64:65], v[32:33]
	v_mov_b64_e32 v[2:3], v[18:19]
	s_mov_b64 s[20:21], s[8:9]
	s_mov_b64 s[22:23], s[6:7]
	s_mov_b64 s[24:25], s[4:5]
	v_mov_b64_e32 v[46:47], v[30:31]
	v_mov_b64_e32 v[44:45], v[28:29]
	v_mov_b64_e32 v[42:43], v[26:27]
	v_mov_b64_e32 v[40:41], v[24:25]
	v_mov_b64_e32 v[38:39], v[22:23]
	v_mov_b64_e32 v[36:37], v[20:21]
	v_mov_b64_e32 v[34:35], v[18:19]
	v_mov_b64_e32 v[62:63], v[30:31]
	v_mov_b64_e32 v[60:61], v[28:29]
	v_mov_b64_e32 v[58:59], v[26:27]
	v_mov_b64_e32 v[56:57], v[24:25]
	v_mov_b64_e32 v[54:55], v[22:23]
	v_mov_b64_e32 v[52:53], v[20:21]
	v_mov_b64_e32 v[50:51], v[18:19]
	v_mov_b64_e32 v[4:5], v[20:21]
	v_mov_b64_e32 v[6:7], v[22:23]
	v_mov_b64_e32 v[8:9], v[24:25]
	v_mov_b64_e32 v[10:11], v[26:27]
	v_mov_b64_e32 v[12:13], v[28:29]
	v_mov_b64_e32 v[14:15], v[30:31]
	v_mov_b64_e32 v[16:17], v[32:33]
	s_waitcnt lgkmcnt(0)
	s_barrier
	v_and_b32_e32 v237, 64, v192
	v_xor_b32_e32 v236, 32, v192
	v_add_u32_e32 v237, 64, v237
	v_cmp_lt_i32_e32 vcc, v236, v237
	s_nop 1
	v_cndmask_b32_e32 v236, v192, v236, vcc
	v_lshlrev_b32_e32 v236, 2, v236

.LBB0_463:
	s_nop 9
	v_max3_f32 v206, v82, v66, s90
	v_max_f32_e32 v208, v83, v67
	v_max3_f32 v206, v206, v84, v68
	v_max3_f32 v208, v208, v85, v69
	v_max3_f32 v206, v206, v86, v70
	v_max3_f32 v208, v208, v87, v71
	v_max3_f32 v206, v206, v88, v72
	v_max3_f32 v208, v208, v89, v73
	v_max3_f32 v206, v206, v90, v74
	v_max3_f32 v208, v208, v91, v75
	v_max3_f32 v206, v206, v92, v76
	v_max3_f32 v208, v208, v93, v77
	v_max3_f32 v206, v206, v94, v78
	v_max3_f32 v208, v208, v95, v79
	v_max3_f32 v206, v206, v96, v80
	v_max3_f32 v208, v208, v97, v81
	v_max_f32_e32 v206, v206, v208
	ds_bpermute_b32 v208, v236, v206
	s_waitcnt lgkmcnt(0)
	v_max3_f32 v206, v207, v206, v208
	v_cmp_neq_f32_e32 vcc, v206, v207
	s_cbranch_vccz .LBB0_465
	v_sub_f32_e32 v207, v207, v206
	v_mul_f32_e32 v207, 0x3dd53b94, v207
	v_exp_f32_e32 v208, v207
	s_nop 0
	v_pk_mul_f32 v[64:65], v[64:65], v[208:209] op_sel_hi:[1,0]
	v_pk_mul_f32 v[62:63], v[62:63], v[208:209] op_sel_hi:[1,0]
	v_pk_mul_f32 v[60:61], v[60:61], v[208:209] op_sel_hi:[1,0]
	v_pk_mul_f32 v[58:59], v[58:59], v[208:209] op_sel_hi:[1,0]
	v_pk_mul_f32 v[56:57], v[56:57], v[208:209] op_sel_hi:[1,0]
	v_pk_mul_f32 v[54:55], v[54:55], v[208:209] op_sel_hi:[1,0]
	v_pk_mul_f32 v[52:53], v[52:53], v[208:209] op_sel_hi:[1,0]
	v_pk_mul_f32 v[50:51], v[50:51], v[208:209] op_sel_hi:[1,0]
	v_pk_mul_f32 v[48:49], v[48:49], v[208:209] op_sel_hi:[1,0]
	v_pk_mul_f32 v[46:47], v[46:47], v[208:209] op_sel_hi:[1,0]
	v_pk_mul_f32 v[44:45], v[44:45], v[208:209] op_sel_hi:[1,0]
	v_pk_mul_f32 v[42:43], v[42:43], v[208:209] op_sel_hi:[1,0]
	v_pk_mul_f32 v[40:41], v[40:41], v[208:209] op_sel_hi:[1,0]
	v_pk_mul_f32 v[38:39], v[38:39], v[208:209] op_sel_hi:[1,0]
	v_pk_mul_f32 v[36:37], v[36:37], v[208:209] op_sel_hi:[1,0]
	v_pk_mul_f32 v[34:35], v[34:35], v[208:209] op_sel_hi:[1,0]
	v_pk_mul_f32 v[32:33], v[32:33], v[208:209] op_sel_hi:[1,0]
	v_pk_mul_f32 v[30:31], v[30:31], v[208:209] op_sel_hi:[1,0]
	v_pk_mul_f32 v[28:29], v[28:29], v[208:209] op_sel_hi:[1,0]
	v_pk_mul_f32 v[26:27], v[26:27], v[208:209] op_sel_hi:[1,0]
	v_pk_mul_f32 v[24:25], v[24:25], v[208:209] op_sel_hi:[1,0]
	v_pk_mul_f32 v[22:23], v[22:23], v[208:209] op_sel_hi:[1,0]
	v_pk_mul_f32 v[20:21], v[20:21], v[208:209] op_sel_hi:[1,0]
	v_pk_mul_f32 v[18:19], v[18:19], v[208:209] op_sel_hi:[1,0]
	v_pk_mul_f32 v[16:17], v[16:17], v[208:209] op_sel_hi:[1,0]
	v_pk_mul_f32 v[14:15], v[14:15], v[208:209] op_sel_hi:[1,0]
	v_pk_mul_f32 v[12:13], v[12:13], v[208:209] op_sel_hi:[1,0]
	v_pk_mul_f32 v[10:11], v[10:11], v[208:209] op_sel_hi:[1,0]
	v_pk_mul_f32 v[8:9], v[8:9], v[208:209] op_sel_hi:[1,0]
	v_pk_mul_f32 v[6:7], v[6:7], v[208:209] op_sel_hi:[1,0]
	v_pk_mul_f32 v[4:5], v[4:5], v[208:209] op_sel_hi:[1,0]
	v_pk_mul_f32 v[2:3], v[2:3], v[208:209] op_sel_hi:[1,0]
	v_mul_f32_e32 v205, v205, v208

.LBB0_476:
	s_nop 9
	v_max3_f32 v207, v82, v66, s90
	v_max_f32_e32 v209, v83, v67
	v_max3_f32 v207, v207, v84, v68
	v_max3_f32 v209, v209, v85, v69
	v_max3_f32 v207, v207, v86, v70
	v_max3_f32 v209, v209, v87, v71
	v_max3_f32 v207, v207, v88, v72
	v_max3_f32 v209, v209, v89, v73
	v_max3_f32 v207, v207, v90, v74
	v_max3_f32 v209, v209, v91, v75
	v_max3_f32 v207, v207, v92, v76
	v_max3_f32 v209, v209, v93, v77
	v_max3_f32 v207, v207, v94, v78
	v_max3_f32 v209, v209, v95, v79
	v_max3_f32 v207, v207, v96, v80
	v_max3_f32 v209, v209, v97, v81
	v_max_f32_e32 v207, v207, v209
	ds_bpermute_b32 v209, v1, v207
	s_waitcnt lgkmcnt(0)
	v_max3_f32 v207, v208, v207, v209
	v_cmp_neq_f32_e32 vcc, v207, v208
	s_cbranch_vccz .LBB0_478
	v_sub_f32_e32 v208, v208, v207
	v_mul_f32_e32 v208, 0x3dd53b94, v208
	v_exp_f32_e32 v208, v208
	s_nop 0
	v_pk_mul_f32 v[64:65], v[64:65], v[208:209] op_sel_hi:[1,0]
	v_pk_mul_f32 v[62:63], v[62:63], v[208:209] op_sel_hi:[1,0]
	v_pk_mul_f32 v[60:61], v[60:61], v[208:209] op_sel_hi:[1,0]
	v_pk_mul_f32 v[58:59], v[58:59], v[208:209] op_sel_hi:[1,0]
	v_pk_mul_f32 v[56:57], v[56:57], v[208:209] op_sel_hi:[1,0]
	v_pk_mul_f32 v[54:55], v[54:55], v[208:209] op_sel_hi:[1,0]
	v_pk_mul_f32 v[52:53], v[52:53], v[208:209] op_sel_hi:[1,0]
	v_pk_mul_f32 v[50:51], v[50:51], v[208:209] op_sel_hi:[1,0]
	v_pk_mul_f32 v[48:49], v[48:49], v[208:209] op_sel_hi:[1,0]
	v_pk_mul_f32 v[46:47], v[46:47], v[208:209] op_sel_hi:[1,0]
	v_pk_mul_f32 v[44:45], v[44:45], v[208:209] op_sel_hi:[1,0]
	v_pk_mul_f32 v[42:43], v[42:43], v[208:209] op_sel_hi:[1,0]
	v_pk_mul_f32 v[40:41], v[40:41], v[208:209] op_sel_hi:[1,0]
	v_pk_mul_f32 v[38:39], v[38:39], v[208:209] op_sel_hi:[1,0]
	v_pk_mul_f32 v[36:37], v[36:37], v[208:209] op_sel_hi:[1,0]
	v_pk_mul_f32 v[34:35], v[34:35], v[208:209] op_sel_hi:[1,0]
	v_pk_mul_f32 v[32:33], v[32:33], v[208:209] op_sel_hi:[1,0]
	v_pk_mul_f32 v[30:31], v[30:31], v[208:209] op_sel_hi:[1,0]
	v_pk_mul_f32 v[28:29], v[28:29], v[208:209] op_sel_hi:[1,0]
	v_pk_mul_f32 v[26:27], v[26:27], v[208:209] op_sel_hi:[1,0]
	v_pk_mul_f32 v[24:25], v[24:25], v[208:209] op_sel_hi:[1,0]
	v_pk_mul_f32 v[22:23], v[22:23], v[208:209] op_sel_hi:[1,0]
	v_pk_mul_f32 v[20:21], v[20:21], v[208:209] op_sel_hi:[1,0]
	v_pk_mul_f32 v[18:19], v[18:19], v[208:209] op_sel_hi:[1,0]
	v_pk_mul_f32 v[16:17], v[16:17], v[208:209] op_sel_hi:[1,0]
	v_pk_mul_f32 v[14:15], v[14:15], v[208:209] op_sel_hi:[1,0]
	v_pk_mul_f32 v[12:13], v[12:13], v[208:209] op_sel_hi:[1,0]
	v_pk_mul_f32 v[10:11], v[10:11], v[208:209] op_sel_hi:[1,0]
	v_pk_mul_f32 v[8:9], v[8:9], v[208:209] op_sel_hi:[1,0]
	v_pk_mul_f32 v[6:7], v[6:7], v[208:209] op_sel_hi:[1,0]
	v_pk_mul_f32 v[4:5], v[4:5], v[208:209] op_sel_hi:[1,0]
	v_pk_mul_f32 v[2:3], v[2:3], v[208:209] op_sel_hi:[1,0]
	v_mul_f32_e32 v205, v205, v208
